# P10 gate/up GEMM K-loop: next-unit gather-index loads no longer followed by s_waitcnt vmcnt(0) inside the LDS-DMA pipeline; loaded into the next-offset registers and waited (vmcnt(2)) at the consumer
# baseline (speedup 1.0000x reference)
.LBB0_1659:
	s_cmpk_eq_i32 s44, 0x700
	s_cselect_b64 s[56:57], -1, 0
	s_and_b64 s[58:59], s[42:43], s[56:57]
	v_cndmask_b32_e64 v2, 0, 1, s[58:59]
	v_cmp_ne_u32_e64 s[2:3], 1, v2
	s_andn2_b64 vcc, exec, s[58:59]
	s_cbranch_vccnz .LBB0_1669
	v_mov_b32_e32 v244, v245
	v_mov_b32_e32 v242, v246
	v_mov_b32_e32 v241, v247
	v_mov_b32_e32 v243, v248
	s_mov_b64 s[58:59], exec
	s_and_b64 exec, s[58:59], s[54:55]
	global_load_dword v244, v[210:211], off
	s_and_b64 exec, s[58:59], s[4:5]
	global_load_dword v242, v[212:213], off
	s_and_b64 exec, s[58:59], s[6:7]
	global_load_dword v241, v[214:215], off
	s_and_b64 exec, s[58:59], s[8:9]
	global_load_dword v243, v[216:217], off
	s_mov_b64 exec, s[58:59]

.Lwx21b:
	s_waitcnt lgkmcnt(0)
	s_barrier
	s_setprio 1
	s_waitcnt lgkmcnt(0)
	v_mfma_scale_f32_16x16x128_f8f6f4 v[190:193], v[18:25], v[34:41], v[190:193], v236, v236 op_sel_hi:[0,0,0]
	v_mfma_scale_f32_16x16x128_f8f6f4 v[186:189], v[26:33], v[34:41], v[186:189], v236, v236 op_sel_hi:[0,0,0]
	v_mfma_scale_f32_16x16x128_f8f6f4 v[182:185], v[18:25], v[42:49], v[182:185], v236, v236 op_sel_hi:[0,0,0]
	v_mfma_scale_f32_16x16x128_f8f6f4 v[178:181], v[26:33], v[42:49], v[178:181], v236, v236 op_sel_hi:[0,0,0]
	v_mfma_scale_f32_16x16x128_f8f6f4 v[174:177], v[18:25], v[50:57], v[174:177], v236, v236 op_sel_hi:[0,0,0]
	v_mfma_scale_f32_16x16x128_f8f6f4 v[170:173], v[26:33], v[50:57], v[170:173], v236, v236 op_sel_hi:[0,0,0]
	v_mfma_scale_f32_16x16x128_f8f6f4 v[166:169], v[18:25], v[58:65], v[166:169], v236, v236 op_sel_hi:[0,0,0]
	v_mfma_scale_f32_16x16x128_f8f6f4 v[162:165], v[26:33], v[58:65], v[162:165], v236, v236 op_sel_hi:[0,0,0]
	s_setprio 0
	s_setprio 1
	v_mfma_scale_f32_16x16x128_f8f6f4 v[158:161], v[2:9], v[34:41], v[158:161], v236, v236 op_sel_hi:[0,0,0]
	v_mfma_scale_f32_16x16x128_f8f6f4 v[154:157], v[10:17], v[34:41], v[154:157], v236, v236 op_sel_hi:[0,0,0]
	v_mfma_scale_f32_16x16x128_f8f6f4 v[150:153], v[2:9], v[42:49], v[150:153], v236, v236 op_sel_hi:[0,0,0]
	v_mfma_scale_f32_16x16x128_f8f6f4 v[146:149], v[10:17], v[42:49], v[146:149], v236, v236 op_sel_hi:[0,0,0]
	v_mfma_scale_f32_16x16x128_f8f6f4 v[142:145], v[2:9], v[50:57], v[142:145], v236, v236 op_sel_hi:[0,0,0]
	v_mfma_scale_f32_16x16x128_f8f6f4 v[138:141], v[10:17], v[50:57], v[138:141], v236, v236 op_sel_hi:[0,0,0]
	v_mfma_scale_f32_16x16x128_f8f6f4 v[134:137], v[2:9], v[58:65], v[134:137], v236, v236 op_sel_hi:[0,0,0]
	v_mfma_scale_f32_16x16x128_f8f6f4 v[130:133], v[10:17], v[58:65], v[130:133], v236, v236 op_sel_hi:[0,0,0]
	s_setprio 0
	s_barrier
	s_and_b64 vcc, exec, s[2:3]
	s_cbranch_vccnz .LBB0_1671
	s_waitcnt vmcnt(2)
	v_lshl_or_b32 v208, v243, 11, v1
	v_lshl_or_b32 v206, v242, 11, v1
	v_lshl_or_b32 v204, v241, 11, v1
	v_lshl_or_b32 v202, v244, 11, v1

.LBB0_1835:
	s_cmpk_eq_i32 s44, 0x700
	s_cselect_b64 s[56:57], -1, 0
	s_and_b64 s[58:59], s[42:43], s[56:57]
	v_cndmask_b32_e64 v2, 0, 1, s[58:59]
	v_cmp_ne_u32_e64 s[2:3], 1, v2
	s_andn2_b64 vcc, exec, s[58:59]
	s_cbranch_vccnz .LBB0_1845
	v_mov_b32_e32 v238, v239
	v_mov_b32_e32 v236, v240
	v_mov_b32_e32 v235, v241
	v_mov_b32_e32 v237, v242
	s_mov_b64 s[58:59], exec
	s_and_b64 exec, s[58:59], s[54:55]
	global_load_dword v238, v[210:211], off
	s_and_b64 exec, s[58:59], s[4:5]
	global_load_dword v236, v[212:213], off
	s_and_b64 exec, s[58:59], s[6:7]
	global_load_dword v235, v[214:215], off
	s_and_b64 exec, s[58:59], s[8:9]
	global_load_dword v237, v[216:217], off
	s_mov_b64 exec, s[58:59]

.Lwx24b:
	s_waitcnt lgkmcnt(0)
	s_barrier
	s_setprio 1
	s_waitcnt lgkmcnt(0)
	v_mfma_scale_f32_16x16x128_f8f6f4 v[190:193], v[18:25], v[34:41], v[190:193], v230, v230 op_sel_hi:[0,0,0]
	v_mfma_scale_f32_16x16x128_f8f6f4 v[186:189], v[26:33], v[34:41], v[186:189], v230, v230 op_sel_hi:[0,0,0]
	v_mfma_scale_f32_16x16x128_f8f6f4 v[182:185], v[18:25], v[42:49], v[182:185], v230, v230 op_sel_hi:[0,0,0]
	v_mfma_scale_f32_16x16x128_f8f6f4 v[178:181], v[26:33], v[42:49], v[178:181], v230, v230 op_sel_hi:[0,0,0]
	v_mfma_scale_f32_16x16x128_f8f6f4 v[174:177], v[18:25], v[50:57], v[174:177], v230, v230 op_sel_hi:[0,0,0]
	v_mfma_scale_f32_16x16x128_f8f6f4 v[170:173], v[26:33], v[50:57], v[170:173], v230, v230 op_sel_hi:[0,0,0]
	v_mfma_scale_f32_16x16x128_f8f6f4 v[166:169], v[18:25], v[58:65], v[166:169], v230, v230 op_sel_hi:[0,0,0]
	v_mfma_scale_f32_16x16x128_f8f6f4 v[162:165], v[26:33], v[58:65], v[162:165], v230, v230 op_sel_hi:[0,0,0]
	s_setprio 0
	s_setprio 1
	v_mfma_scale_f32_16x16x128_f8f6f4 v[158:161], v[2:9], v[34:41], v[158:161], v230, v230 op_sel_hi:[0,0,0]
	v_mfma_scale_f32_16x16x128_f8f6f4 v[154:157], v[10:17], v[34:41], v[154:157], v230, v230 op_sel_hi:[0,0,0]
	v_mfma_scale_f32_16x16x128_f8f6f4 v[150:153], v[2:9], v[42:49], v[150:153], v230, v230 op_sel_hi:[0,0,0]
	v_mfma_scale_f32_16x16x128_f8f6f4 v[146:149], v[10:17], v[42:49], v[146:149], v230, v230 op_sel_hi:[0,0,0]
	v_mfma_scale_f32_16x16x128_f8f6f4 v[142:145], v[2:9], v[50:57], v[142:145], v230, v230 op_sel_hi:[0,0,0]
	v_mfma_scale_f32_16x16x128_f8f6f4 v[138:141], v[10:17], v[50:57], v[138:141], v230, v230 op_sel_hi:[0,0,0]
	v_mfma_scale_f32_16x16x128_f8f6f4 v[134:137], v[2:9], v[58:65], v[134:137], v230, v230 op_sel_hi:[0,0,0]
	v_mfma_scale_f32_16x16x128_f8f6f4 v[130:133], v[10:17], v[58:65], v[130:133], v230, v230 op_sel_hi:[0,0,0]
	s_setprio 0
	s_barrier
	s_and_b64 vcc, exec, s[2:3]
	s_cbranch_vccnz .LBB0_1847
	s_waitcnt vmcnt(2)
	v_lshl_or_b32 v208, v237, 11, v1
	v_lshl_or_b32 v206, v236, 11, v1
	v_lshl_or_b32 v204, v235, 11, v1
	v_lshl_or_b32 v202, v238, 11, v1
